# queue order: every workgroup takes its expert-conversion batch right after its MLA unit (the differential units are statically assigned now, so nothing is gained by rushing to that queue first)
# baseline (speedup 1.0000x reference)
;     ...
;     const bool conv_now = (qs == 0 && l + 1 < L && lastm < 128);
;     if (conv_now) attn_conv_batches(lds, wv, l, 1);
.LBB0_894:
	s_cmp_lt_i32 s72, 3
	s_cselect_b64 s[2:3], -1, 0
	s_cmpk_lt_i32 s28, 0x100
	s_cselect_b64 s[48:49], -1, 0
	v_writelane_b32 v255, s2, 9
	s_mov_b64 s[14:15], -1
	s_nop 0
	v_writelane_b32 v255, s3, 10
	s_and_b64 s[2:3], s[2:3], s[48:49]
	s_and_b64 vcc, exec, s[2:3]
	s_cbranch_vccnz .LBB0_896
	s_lshl_b32 s10, s72, 4
	s_ashr_i32 s11, s10, 31
	s_mov_b64 s[14:15], 0
